# grid barrier: leaders add TOP without return, every WG polls TOP >= (gen+1)*nx directly (drops TOPGEN and XGEN stages)
# baseline (speedup 1.0000x reference)
.LBB0_59:
	v_readlane_b32 s100, v254, 4
	v_readlane_b32 s101, v254, 5
	v_readlane_b32 vcc_lo, v254, 6
	v_mov_b32_e32 v3, 0x1000
	s_lshl_b32 vcc_lo, vcc_lo, 8
	v_mov_b32_e32 v4, 1
	v_add_u32_e32 v3, vcc_lo, v3
	v_mov_b32_e32 v1, 0x20160
	s_nop 4
	global_atomic_add v3, v3, v4, s[100:101] offset:1024 sc0
	ds_read_b32 v2, v1
	ds_read_b32 v1, v1 offset:4
	s_waitcnt lgkmcnt(0)
	v_cvt_f32_u32_e32 v5, v2
	v_rcp_f32_e32 v5, v5
	s_waitcnt vmcnt(0)
	v_cvt_f32_u32_e32 v0, v3
	v_add_f32_e32 v0, 0.5, v0
	v_mul_f32_e32 v0, v0, v5
	v_cvt_u32_f32_e32 v0, v0
	v_add_u32_e32 v0, 1, v0
	v_mul_lo_u32 v5, v0, v2
	v_add_u32_e32 v3, 1, v3
	v_mul_lo_u32 v0, v0, v1
	v_cmp_eq_u32_e32 vcc, v3, v5
	v_mov_b32_e32 v3, 0x3000
	v_mov_b32_e32 v2, 0
	s_cbranch_vccz .Lmy_bar0_spin
	buffer_wbl2 sc1
	s_waitcnt vmcnt(0)
	global_atomic_add v3, v4, s[100:101] offset:1024
.Lmy_bar0_spin:
	global_load_dword v5, v3, s[100:101] offset:1024 sc1
	s_waitcnt vmcnt(0)
	v_cmp_ge_u32_e32 vcc, v5, v0
	s_cbranch_vccnz .Lmy_bar0_done
	s_sleep 1
	v_add_u32_e32 v2, 1, v2
	v_cmp_gt_u32_e32 vcc, 0x2000, v2
	s_cbranch_vccnz .Lmy_bar0_spin
.Lmy_bar0_done:
	buffer_inv sc1
	s_waitcnt vmcnt(0)

.LBB0_261:
	v_readlane_b32 s100, v254, 4
	v_readlane_b32 s101, v254, 5
	v_readlane_b32 vcc_lo, v254, 6
	v_mov_b32_e32 v3, 0x1000
	s_lshl_b32 vcc_lo, vcc_lo, 8
	v_mov_b32_e32 v4, 1
	v_add_u32_e32 v3, vcc_lo, v3
	v_mov_b32_e32 v1, 0x20160
	s_nop 4
	global_atomic_add v3, v3, v4, s[100:101] offset:1024 sc0
	ds_read_b32 v2, v1
	ds_read_b32 v1, v1 offset:4
	s_waitcnt lgkmcnt(0)
	v_cvt_f32_u32_e32 v5, v2
	v_rcp_f32_e32 v5, v5
	s_waitcnt vmcnt(0)
	v_cvt_f32_u32_e32 v6, v3
	v_add_f32_e32 v6, 0.5, v6
	v_mul_f32_e32 v6, v6, v5
	v_cvt_u32_f32_e32 v6, v6
	v_add_u32_e32 v6, 1, v6
	v_mul_lo_u32 v5, v6, v2
	v_add_u32_e32 v3, 1, v3
	v_mul_lo_u32 v6, v6, v1
	v_cmp_eq_u32_e32 vcc, v3, v5
	v_mov_b32_e32 v3, 0x3000
	v_mov_b32_e32 v2, 0
	s_cbranch_vccz .Lmy_bar2_spin
	buffer_wbl2 sc1
	s_waitcnt vmcnt(0)
	global_atomic_add v3, v4, s[100:101] offset:1024
.Lmy_bar2_spin:
	global_load_dword v5, v3, s[100:101] offset:1024 sc1
	s_waitcnt vmcnt(0)
	v_cmp_ge_u32_e32 vcc, v5, v6
	s_cbranch_vccnz .Lmy_bar2_done
	s_sleep 1
	v_add_u32_e32 v2, 1, v2
	v_cmp_gt_u32_e32 vcc, 0x2000, v2
	s_cbranch_vccnz .Lmy_bar2_spin

.Lmy_bar15_done:
	buffer_inv sc1
	s_waitcnt vmcnt(0)
	s_mov_b64 s[6:7], 0
	s_getpc_b64 s[98:99]
